# v023
# speedup vs baseline: 1.0493x; 1.0493x over previous
.LBB1_8:
	s_or_b64 exec, exec, s[12:13]
	s_mov_b32 s14, 0
	v_cmp_eq_u32_e32 vcc, 0, v0
	s_and_saveexec_b64 s[0:1], vcc
	v_mov_b32_e32 v1, 0
	ds_write_b32 v1, v1 offset:24832
	s_or_b64 exec, exec, s[0:1]
	s_lshr_b32 s0, s2, 1
	s_and_b32 s0, s0, 0x7fffffc
	s_and_b32 s1, s2, 3
	s_or_b32 s0, s0, s1
	s_bfe_u32 s16, s2, 0x10002
	s_lshl_b32 s2, s0, 5
	s_ashr_i32 s3, s2, 31
	s_lshl_b64 s[0:1], s[2:3], 7
	s_waitcnt lgkmcnt(0)
	s_add_u32 s0, s8, s0
	s_addc_u32 s1, s9, s1
	s_add_u32 s4, s0, 0x49000
	s_addc_u32 s5, s1, 0
	v_add_u32_e32 v5, 1, v2
	s_cmp_eq_u32 s16, 0
	v_lshlrev_b32_e32 v1, 9, v5
	s_cselect_b64 vcc, -1, 0
	v_add_u32_e32 v2, 0x4080, v6
	v_sub_u32_e32 v4, 0, v0
	v_and_b32_e32 v3, 0x3800, v1
	s_mov_b64 s[6:7], 0
	v_mov_b32_e32 v1, 0
	s_movk_i32 s15, 0xff7e
	s_movk_i32 s17, 0x80
	s_mov_b32 s18, 0
	s_barrier
	v_lshlrev_b32_e32 v1, 3, v0
	global_load_dwordx2 v[2:3], v1, s[4:5]
	v_lshrrev_b32_e32 v4, 4, v0
	v_and_b32_e32 v5, 15, v0
	v_mul_u32_u24_e32 v4, 0x104, v4
	v_lshlrev_b32_e32 v5, 4, v5
	v_mov_b32_e32 v6, 0x4000400
	ds_write_b32 v4, v6 offset:16768
	s_waitcnt vmcnt(0)
	s_mov_b32 s0, 0xe0e0e0e0
	s_mov_b32 s1, 0x20202020
	s_mov_b32 s6, 0x01010101
	s_mov_b32 s7, 0x80808080
	v_and_b32_e32 v7, s0, v2
	v_xor_b32_e32 v7, s1, v7
	v_subrev_u32_e32 v9, s6, v7
	v_not_b32_e32 v7, v7
	v_and_b32_e32 v7, v9, v7
	v_and_b32_e32 v7, s7, v7
	v_and_b32_e32 v8, s0, v3
	v_xor_b32_e32 v8, s1, v8
	v_subrev_u32_e32 v9, s6, v8
	v_not_b32_e32 v8, v8
	v_and_b32_e32 v8, v9, v8
	v_and_b32_e32 v8, s7, v8
	v_or_b32_e32 v7, v7, v8
	v_bfe_u32 v8, v2, 0, 8
	v_bfe_u32 v9, v2, 8, 8
	v_min_u32_e32 v8, 64, v8
	v_min_u32_e32 v9, 64, v9
	v_lshlrev_b32_e32 v8, 4, v8
	v_lshlrev_b32_e32 v9, 20, v9
	v_or_b32_e32 v10, v8, v9
	v_bfe_u32 v8, v2, 16, 8
	v_bfe_u32 v9, v2, 24, 8
	v_min_u32_e32 v8, 64, v8
	v_min_u32_e32 v9, 64, v9
	v_lshlrev_b32_e32 v8, 4, v8
	v_lshlrev_b32_e32 v9, 20, v9
	v_or_b32_e32 v11, v8, v9
	v_bfe_u32 v8, v3, 0, 8
	v_bfe_u32 v9, v3, 8, 8
	v_min_u32_e32 v8, 64, v8
	v_min_u32_e32 v9, 64, v9
	v_lshlrev_b32_e32 v8, 4, v8
	v_lshlrev_b32_e32 v9, 20, v9
	v_or_b32_e32 v12, v8, v9
	v_bfe_u32 v8, v3, 16, 8
	v_bfe_u32 v9, v3, 24, 8
	v_min_u32_e32 v8, 64, v8
	v_min_u32_e32 v9, 64, v9
	v_lshlrev_b32_e32 v8, 4, v8
	v_lshlrev_b32_e32 v9, 20, v9
	v_or_b32_e32 v13, v8, v9
	s_cmp_eq_u32 s16, 0
	s_cbranch_scc0 .Ltok_bwd
	v_add_u32_e32 v4, v4, v5
	ds_write_b32 v4, v10 offset:16512
	ds_write_b32 v4, v11 offset:16516
	ds_write_b32 v4, v12 offset:16520
	ds_write_b32 v4, v13 offset:16524
	s_branch .Ltok_done
.Ltok_bwd:
	v_sub_u32_e32 v4, v4, v5
	v_alignbit_b32 v10, v10, v10, 16
	v_alignbit_b32 v11, v11, v11, 16
	v_alignbit_b32 v12, v12, v12, 16
	v_alignbit_b32 v13, v13, v13, 16
	ds_write_b32 v4, v13 offset:16752
	ds_write_b32 v4, v12 offset:16756
	ds_write_b32 v4, v11 offset:16760
	ds_write_b32 v4, v10 offset:16764
.Ltok_done:
	v_cmp_ne_u32_e32 vcc, 0, v7
	s_and_saveexec_b64 s[6:7], vcc
	v_mov_b32_e32 v1, 1
	v_mov_b32_e32 v2, 0
	ds_write_b32 v2, v1 offset:24832
	s_or_b64 exec, exec, s[6:7]
	s_mov_b32 s5, 0
	s_cmp_eq_u32 s16, 0
	s_cselect_b64 vcc, -1, 0
	v_mov_b32_e32 v157, 0
	s_waitcnt lgkmcnt(0)
	s_barrier
	ds_read_b32 v1, v157 offset:24832
	v_lshrrev_b32_e32 v108, 6, v0
	v_and_b32_e32 v4, 63, v0
	s_movk_i32 s0, 0x1000
	v_mov_b32_e32 v9, v157
	s_waitcnt lgkmcnt(0)
	v_readfirstlane_b32 s4, v1
	v_lshl_or_b32 v1, s16, 3, v108
	v_mul_u32_u24_e32 v1, 0x300, v1
	v_lshlrev_b32_e32 v156, 4, v1
	v_lshl_add_u64 v[2:3], s[8:9], 0, v[156:157]
	v_lshlrev_b32_e32 v156, 4, v4
	v_lshl_add_u64 v[2:3], v[2:3], 0, v[156:157]
	v_add_co_u32_e64 v4, s[0:1], s0, v2
	v_lshl_or_b32 v1, s16, 4, v108
	s_nop 0
	v_addc_co_u32_e64 v5, s[0:1], 0, v3, s[0:1]
	s_movk_i32 s0, 0x2000
	s_nop 0
	v_add_co_u32_e64 v6, s[0:1], s0, v2
	v_or_b32_e32 v8, 8, v1
	s_nop 0
	v_addc_co_u32_e64 v7, s[0:1], 0, v3, s[0:1]
	s_add_u32 s0, s8, 0x30000
	v_mul_u32_u24_e32 v8, 0xc0, v8
	s_addc_u32 s1, s9, 0
	v_lshlrev_b32_e32 v8, 4, v8
	v_mul_u32_u24_e32 v1, 0xc0, v1
	v_lshl_add_u64 v[92:93], s[0:1], 0, v[8:9]
	v_lshlrev_b32_e32 v8, 4, v1
	s_cmp_lg_u32 s4, 0
	v_lshl_add_u64 v[8:9], s[0:1], 0, v[8:9]
	s_cselect_b64 s[12:13], -1, 0
	s_lshl_b32 s0, s16, 11
	s_add_u32 s0, s8, s0
	s_addc_u32 s1, s9, 0
	v_and_b32_e32 v10, 0x1c0, v0
	v_mov_b32_e32 v11, v157
	v_lshl_add_u64 v[10:11], s[0:1], 0, v[10:11]
	v_and_b32_e32 v12, 48, v0
	v_mov_b32_e32 v13, v157
	v_and_b32_e32 v161, 15, v0
	v_lshl_add_u64 v[10:11], v[10:11], 0, v[12:13]
	s_mov_b64 s[0:1], 0x48000
	v_lshrrev_b32_e32 v12, 5, v0
	v_bfe_u32 v13, v0, 5, 1
	v_bfe_u32 v109, v0, 4, 2
	v_lshl_add_u64 v[72:73], v[10:11], 0, s[0:1]
	s_mov_b32 s0, 0x48000
	v_lshlrev_b32_e32 v1, 3, v0
	v_and_or_b32 v12, v12, 2, v13
	v_lshlrev_b32_e32 v13, 4, v161
	v_lshrrev_b32_e32 v0, 1, v0
	v_add_co_u32_e64 v10, s[0:1], s0, v10
	v_and_b32_e32 v1, 0xc00, v1
	v_lshl_or_b32 v12, v12, 8, v13
	v_and_b32_e32 v0, 8, v0
	v_lshl_add_u64 v[8:9], v[8:9], 0, v[156:157]
	v_addc_co_u32_e64 v11, s[0:1], 0, v11, s[0:1]
	v_or3_b32 v163, v12, v1, v0
	global_load_dwordx4 v[12:15], v[2:3], off
	global_load_dwordx4 v[16:19], v[2:3], off offset:1024
	global_load_dwordx4 v[20:23], v[2:3], off offset:2048
	global_load_dwordx4 v[24:27], v[2:3], off offset:3072
	global_load_dwordx4 v[28:31], v[6:7], off offset:-4096
	global_load_dwordx4 v[32:35], v[6:7], off
	global_load_dwordx4 v[36:39], v[6:7], off offset:1024
	global_load_dwordx4 v[40:43], v[6:7], off offset:2048
	global_load_dwordx4 v[44:47], v[6:7], off offset:3072
	global_load_dwordx4 v[48:51], v[4:5], off offset:1024
	global_load_dwordx4 v[52:55], v[4:5], off offset:2048
	global_load_dwordx4 v[56:59], v[4:5], off offset:3072
	global_load_dwordx4 v[60:63], v[8:9], off
	global_load_dwordx4 v[64:67], v[8:9], off offset:1024
	global_load_dwordx4 v[68:71], v[8:9], off offset:2048
	global_load_dwordx4 v[76:79], v[72:73], off offset:512
	global_load_dwordx4 v[80:83], v[72:73], off offset:1024
	global_load_dwordx4 v[84:87], v[10:11], off
	global_load_dwordx4 v[88:91], v[72:73], off offset:1536
	s_and_b64 s[0:1], vcc, exec
	s_cselect_b32 s14, 0, 0x7f
	s_lshl_b32 s7, s16, 22
	s_add_u32 s0, s8, s7
	s_addc_u32 s1, s9, 0
	v_lshlrev_b32_e32 v94, 12, v108
	v_mov_b32_e32 v95, v157
	v_lshl_add_u64 v[0:1], s[0:1], 0, v[94:95]
	v_lshl_add_u64 v[0:1], v[0:1], 0, v[156:157]
	s_mov_b64 s[0:1], 0xc9000
	v_lshl_add_u64 v[158:159], v[0:1], 0, s[0:1]
	s_lshl_b32 s4, s14, 15
	v_lshl_add_u64 v[96:97], v[158:159], 0, s[4:5]
	global_load_dwordx4 v[72:75], v[96:97], off
	global_load_dwordx4 v[8:11], v[96:97], off offset:1024
	global_load_dwordx4 v[4:7], v[96:97], off offset:2048
	global_load_dwordx4 v[0:3], v[96:97], off offset:3072
	v_mul_u32_u24_e32 v95, 0x104, v161
	ds_read_b32 v96, v95 offset:16512
	ds_read_b32 v95, v95 offset:20672
	s_movk_i32 s6, 0x410
	s_movk_i32 s0, 0x104
	v_mov_b32_e32 v97, 0x4080
	s_waitcnt lgkmcnt(1)
	v_lshrrev_b32_e32 v178, 16, v96
	v_and_b32_e32 v96, 0xffff, v96
	v_mad_u32_u24 v176, v161, s0, v97
	v_mad_u32_u24 v110, v109, s6, v96
	s_waitcnt lgkmcnt(0)
	v_lshrrev_b32_e32 v177, 16, v95
	v_and_b32_e32 v95, 0xffff, v95
	s_and_b64 s[0:1], vcc, exec
	v_mad_u32_u24 v111, v109, s6, v95
	s_cselect_b32 s15, 1, -1
	s_or_b32 s0, s7, s4
	ds_read_b128 v[120:123], v110 offset:8192
	ds_read_b128 v[116:119], v111 offset:8192
	v_lshl_add_u64 v[164:165], v[92:93], 0, v[156:157]
	v_or3_b32 v92, s0, v94, v156
	v_mov_b32_e32 v93, v157
	v_lshl_add_u64 v[92:93], s[8:9], 0, v[92:93]
	s_mov_b64 s[0:1], 0xc9800
	s_lshl_b32 s4, s15, 1
	v_mov_b32_e32 v106, v157
	v_mov_b32_e32 v107, v157
	v_lshl_add_u64 v[166:167], v[92:93], 0, s[0:1]
	s_ashr_i32 s5, s4, 31
	v_mov_b32_e32 v100, 0xc47a0000
	v_mov_b32_e32 v104, v157
	v_mov_b32_e32 v105, v157
	v_cndmask_b32_e64 v92, 0, 1, s[12:13]
	v_mov_b64_e32 v[142:143], v[106:107]
	s_lshl_b64 s[6:7], s[4:5], 15
	s_add_i32 s8, s14, s15
	v_mov_b32_e32 v101, v100
	v_mov_b32_e32 v102, v100
	v_mov_b32_e32 v103, v100
	s_mov_b32 s5, -2
	v_cmp_ne_u32_e64 s[0:1], 1, v92
	v_mov_b32_e32 v172, v157
	v_mov_b32_e32 v173, v157
	v_mov_b32_e32 v174, v157
	v_mov_b32_e32 v175, v157
	v_mov_b32_e32 v96, v157
	v_mov_b32_e32 v97, v157
	v_mov_b32_e32 v98, v157
	v_mov_b32_e32 v99, v157
	v_mov_b32_e32 v92, v157
	v_mov_b32_e32 v93, v157
	v_mov_b32_e32 v94, v157
	v_mov_b32_e32 v95, v157
	v_mov_b32_e32 v144, v157
	v_mov_b32_e32 v145, v157
	v_mov_b32_e32 v146, v157
	v_mov_b32_e32 v147, v157
	v_mov_b32_e32 v132, v157
	v_mov_b32_e32 v133, v157
	v_mov_b32_e32 v134, v157
	v_mov_b32_e32 v135, v157
	v_mov_b32_e32 v128, v157
	v_mov_b32_e32 v129, v157
	v_mov_b32_e32 v130, v157
	v_mov_b32_e32 v131, v157
	v_mov_b32_e32 v136, v157
	v_mov_b32_e32 v137, v157
	v_mov_b32_e32 v138, v157
	v_mov_b32_e32 v139, v157
	v_mov_b32_e32 v124, v157
	v_mov_b32_e32 v125, v157
	v_mov_b32_e32 v126, v157
	v_mov_b32_e32 v127, v157
	v_mov_b32_e32 v170, v157
	v_mov_b32_e32 v171, v157
	v_mov_b32_e32 v168, v157
	v_mov_b32_e32 v169, v157
	v_lshlrev_b32_e32 v162, 4, v108
	v_mul_u32_u24_e32 v157, 0x410, v109
	v_lshlrev_b32_e32 v160, 2, v109
	v_mov_b64_e32 v[140:141], v[104:105]
	v_mov_b32_e32 v144, 0
	v_mov_b32_e32 v145, 0
	v_mov_b32_e32 v146, 0
	v_mov_b32_e32 v147, 0
	v_mov_b32_e32 v148, 0xc47a0000
	v_mov_b32_e32 v149, 0xc47a0000
	v_mov_b32_e32 v150, 0xc47a0000
	v_mov_b32_e32 v151, 0xc47a0000
	v_mov_b32_e32 v152, 0
	v_mov_b32_e32 v153, 0
	v_mov_b32_e32 v154, 0
	v_mov_b32_e32 v155, 0
	s_movk_i32 s17, 0x61
	global_load_dwordx4 v[206:209], v[164:165], off
	global_load_dwordx4 v[210:213], v[164:165], off offset:1024
	global_load_dwordx4 v[214:217], v[164:165], off offset:2048
	v_add_u32_e32 v252, v162, v160
	v_mul_u32_u24_e32 v252, 12, v252
	v_lshl_add_u32 v229, v161, 4, v157
	v_mul_u32_u24_e32 v230, 0x610, v161
	v_add_u32_e32 v230, v230, v252
	v_add_u32_e32 v231, 0x18400, v252
	s_waitcnt vmcnt(0) lgkmcnt(0)
	ds_read_b128 v[190:193], v229 offset:8192
	s_waitcnt lgkmcnt(0)
	v_mfma_f32_16x16x32_f16 v[194:197], v[60:63], v[190:193], v[84:87]
	v_mfma_f32_16x16x32_f16 v[198:201], v[64:67], v[190:193], v[76:79]
	v_mfma_f32_16x16x32_f16 v[202:205], v[68:71], v[190:193], v[88:91]
	s_nop 7
	s_nop 1
	ds_write_b128 v230, v[194:197] offset:24848
	ds_write_b128 v230, v[198:201] offset:24864
	ds_write_b128 v230, v[202:205] offset:24880
	v_add_u32_e32 v230, 0x6100, v230
	ds_read_b128 v[190:193], v229 offset:8448
	s_waitcnt lgkmcnt(0)
	v_mfma_f32_16x16x32_f16 v[194:197], v[60:63], v[190:193], v[84:87]
	v_mfma_f32_16x16x32_f16 v[198:201], v[64:67], v[190:193], v[76:79]
	v_mfma_f32_16x16x32_f16 v[202:205], v[68:71], v[190:193], v[88:91]
	s_nop 7
	s_nop 1
	ds_write_b128 v230, v[194:197] offset:24848
	ds_write_b128 v230, v[198:201] offset:24864
	ds_write_b128 v230, v[202:205] offset:24880
	v_add_u32_e32 v230, 0x6100, v230
	ds_read_b128 v[190:193], v229 offset:12864
	s_waitcnt lgkmcnt(0)
	v_mfma_f32_16x16x32_f16 v[194:197], v[206:209], v[190:193], v[84:87]
	v_mfma_f32_16x16x32_f16 v[198:201], v[210:213], v[190:193], v[76:79]
	v_mfma_f32_16x16x32_f16 v[202:205], v[214:217], v[190:193], v[88:91]
	s_nop 7
	s_nop 1
	ds_write_b128 v230, v[194:197] offset:24848
	ds_write_b128 v230, v[198:201] offset:24864
	ds_write_b128 v230, v[202:205] offset:24880
	v_add_u32_e32 v230, 0x6100, v230
	ds_read_b128 v[190:193], v229 offset:13120
	s_waitcnt lgkmcnt(0)
	v_mfma_f32_16x16x32_f16 v[194:197], v[206:209], v[190:193], v[84:87]
	v_mfma_f32_16x16x32_f16 v[198:201], v[210:213], v[190:193], v[76:79]
	v_mfma_f32_16x16x32_f16 v[202:205], v[214:217], v[190:193], v[88:91]
	s_nop 7
	s_nop 1
	ds_write_b128 v230, v[194:197] offset:24848
	ds_write_b128 v230, v[198:201] offset:24864
	ds_write_b128 v230, v[202:205] offset:24880
	ds_write_b128 v231, v[84:87] offset:24848
	ds_write_b128 v231, v[76:79] offset:24864
	ds_write_b128 v231, v[88:91] offset:24880
	ds_read_u16 v232, v176
	ds_read_u16 v177, v176 offset:4160
	s_waitcnt lgkmcnt(0)
	v_mad_u32_u24 v253, v232, s17, v252
	ds_read_b128 v[116:119], v253 offset:24848
	ds_read_b128 v[120:123], v253 offset:24864
	ds_read_b128 v[138:141], v253 offset:24880
	v_mov_b32_e32 v182, 0
	v_mov_b32_e32 v183, 0
	v_mov_b32_e32 v184, 0
	v_mov_b32_e32 v185, 0
	v_mov_b32_e32 v222, 0
	v_mov_b32_e32 v223, 0
	v_mov_b32_e32 v224, 0
	v_mov_b32_e32 v225, 0
	v_mov_b32_e32 v186, 0
	v_mov_b32_e32 v187, 0
	v_mov_b32_e32 v188, 0
	v_mov_b32_e32 v189, 0
	v_mov_b32_e32 v100, 0
	v_mov_b32_e32 v101, 0
	v_mov_b32_e32 v102, 0
	v_mov_b32_e32 v103, 0
	v_mov_b32_e32 v104, 0
	v_mov_b32_e32 v105, 0
	v_mov_b32_e32 v106, 0
	v_mov_b32_e32 v107, 0
	v_mov_b32_e32 v108, 0
	v_mov_b32_e32 v109, 0
	v_mov_b32_e32 v110, 0
	v_mov_b32_e32 v111, 0
	v_mov_b32_e32 v112, 0
	v_mov_b32_e32 v113, 0
	v_mov_b32_e32 v114, 0
	v_mov_b32_e32 v115, 0
	v_mov_b32_e32 v206, 0
	v_mov_b32_e32 v207, 0
	v_mov_b32_e32 v208, 0
	v_mov_b32_e32 v209, 0
	v_mov_b32_e32 v210, 0
	v_mov_b32_e32 v211, 0
	v_mov_b32_e32 v212, 0
	v_mov_b32_e32 v213, 0
	v_mov_b32_e32 v214, 0
	v_mov_b32_e32 v215, 0
	v_mov_b32_e32 v216, 0
	v_mov_b32_e32 v217, 0
	v_mov_b32_e32 v218, 0
	v_mov_b32_e32 v219, 0
	v_mov_b32_e32 v220, 0
	v_mov_b32_e32 v221, 0
	s_waitcnt vmcnt(4) lgkmcnt(0)
.Lgru_loop:
	ds_read_b128 v[190:193], v156 offset:0
	ds_read_b128 v[194:197], v156 offset:1024
	ds_read_b128 v[198:201], v156 offset:2048
	ds_read_b128 v[202:205], v156 offset:3072
	s_waitcnt vmcnt(4)
	v_mfma_f32_16x16x32_f16 v[92:95], v[112:115], v[206:209], v[92:95]
	v_exp_f32_e32 v228, v144
	v_exp_f32_e32 v229, v145
	v_exp_f32_e32 v230, v146
	v_mfma_f32_16x16x32_f16 v[92:95], v[108:111], v[210:213], v[92:95]
	v_exp_f32_e32 v231, v147
	v_exp_f32_e32 v232, v148
	v_exp_f32_e32 v233, v149
	v_mfma_f32_16x16x32_f16 v[92:95], v[104:107], v[214:217], v[92:95]
	v_exp_f32_e32 v234, v150
	v_exp_f32_e32 v235, v151
	v_add_f32_e32 v228, 1.0, v228
	v_add_f32_e32 v229, 1.0, v229
	v_mfma_f32_16x16x32_f16 v[92:95], v[100:103], v[218:221], v[92:95]
	global_load_dwordx4 v[112:115], v[166:167], off offset:-2048
	global_load_dwordx4 v[108:111], v[166:167], off offset:-1024
	global_load_dwordx4 v[104:107], v[166:167], off
	global_load_dwordx4 v[100:103], v[166:167], off offset:1024
	v_add_f32_e32 v230, 1.0, v230
	v_add_f32_e32 v231, 1.0, v231
	v_add_f32_e32 v232, 1.0, v232
	v_add_f32_e32 v233, 1.0, v233
	v_add_f32_e32 v234, 1.0, v234
	v_add_f32_e32 v235, 1.0, v235
	s_waitcnt lgkmcnt(3)
	v_mfma_f32_16x16x32_f16 v[124:127], v[12:15], v[190:193], v[116:119]
	v_rcp_f32_e32 v228, v228
	v_rcp_f32_e32 v229, v229
	v_rcp_f32_e32 v230, v230
	v_mfma_f32_16x16x32_f16 v[128:131], v[28:31], v[190:193], v[120:123]
	v_rcp_f32_e32 v231, v231
	v_fma_f32 v236, v228, v152, v182
	v_fma_f32 v237, v229, v153, v183
	v_fma_f32 v238, v230, v154, v184
	v_fma_f32 v239, v231, v155, v185
	v_mfma_f32_16x16x32_f16 v[132:135], v[32:35], v[190:193], v[80:83]
	v_mad_u32_u24 v253, v177, s17, v252
	ds_read_b128 v[222:225], v253 offset:24848
	ds_read_b128 v[186:189], v253 offset:24864
	ds_read_b128 v[182:185], v253 offset:24880
	ds_read_u16 v177, v176 offset:4162
	v_exp_f32_e32 v236, v236
	v_exp_f32_e32 v237, v237
	v_exp_f32_e32 v238, v238
	s_waitcnt lgkmcnt(6)
	v_mfma_f32_16x16x32_f16 v[124:127], v[16:19], v[194:197], v[124:127]
	v_exp_f32_e32 v239, v239
	v_rcp_f32_e32 v232, v232
	v_rcp_f32_e32 v233, v233
	v_mfma_f32_16x16x32_f16 v[128:131], v[48:51], v[194:197], v[128:131]
	v_rcp_f32_e32 v234, v234
	v_rcp_f32_e32 v235, v235
	v_add_f32_e32 v236, 1.0, v236
	v_add_f32_e32 v237, 1.0, v237
	v_mfma_f32_16x16x32_f16 v[132:135], v[36:39], v[194:197], v[132:135]
	v_add_f32_e32 v238, 1.0, v238
	v_add_f32_e32 v239, 1.0, v239
	v_rcp_f32_e32 v236, v236
	v_rcp_f32_e32 v237, v237
	s_waitcnt lgkmcnt(5)
	v_mfma_f32_16x16x32_f16 v[124:127], v[20:23], v[198:201], v[124:127]
	v_rcp_f32_e32 v238, v238
	v_rcp_f32_e32 v239, v239
	v_pk_fma_f32 v[236:237], v[236:237], -2.0, 1.0 op_sel_hi:[1,0,0]
	v_pk_fma_f32 v[238:239], v[238:239], -2.0, 1.0 op_sel_hi:[1,0,0]
	v_mfma_f32_16x16x32_f16 v[128:131], v[52:55], v[198:201], v[128:131]
	v_pk_add_f32 v[240:241], v[168:169], v[236:237] neg_lo:[0,1] neg_hi:[0,1]
	v_pk_add_f32 v[242:243], v[170:171], v[238:239] neg_lo:[0,1] neg_hi:[0,1]
	v_pk_fma_f32 v[168:169], v[232:233], v[240:241], v[236:237]
	v_pk_fma_f32 v[170:171], v[234:235], v[242:243], v[238:239]
	v_cvt_pk_f16_f32 v244, v168, v169
	v_cvt_pk_f16_f32 v245, v170, v171
	ds_write_b64 v163, v[244:245] offset:4096
	v_mfma_f32_16x16x32_f16 v[132:135], v[40:43], v[198:201], v[132:135]
	s_waitcnt lgkmcnt(5)
	v_mfma_f32_16x16x32_f16 v[124:127], v[24:27], v[202:205], v[124:127]
	v_mfma_f32_16x16x32_f16 v[128:131], v[56:59], v[202:205], v[128:131]
	v_mfma_f32_16x16x32_f16 v[132:135], v[44:47], v[202:205], v[132:135]
	s_waitcnt lgkmcnt(0)
	s_barrier
	ds_read_b128 v[206:209], v156 offset:4096
	ds_read_b128 v[210:213], v156 offset:5120
	ds_read_b128 v[214:217], v156 offset:6144
	ds_read_b128 v[218:221], v156 offset:7168
	s_waitcnt vmcnt(4)
	v_mfma_f32_16x16x32_f16 v[96:99], v[72:75], v[190:193], v[96:99]
	v_exp_f32_e32 v228, v124
	v_exp_f32_e32 v229, v125
	v_exp_f32_e32 v230, v126
	v_mfma_f32_16x16x32_f16 v[96:99], v[8:11], v[194:197], v[96:99]
	v_exp_f32_e32 v231, v127
	v_exp_f32_e32 v232, v128
	v_exp_f32_e32 v233, v129
	v_mfma_f32_16x16x32_f16 v[96:99], v[4:7], v[198:201], v[96:99]
	v_exp_f32_e32 v234, v130
	v_exp_f32_e32 v235, v131
	v_add_f32_e32 v228, 1.0, v228
	v_add_f32_e32 v229, 1.0, v229
	v_mfma_f32_16x16x32_f16 v[96:99], v[0:3], v[202:205], v[96:99]
	v_add_f32_e32 v230, 1.0, v230
	v_add_f32_e32 v231, 1.0, v231
	v_add_f32_e32 v232, 1.0, v232
	v_add_f32_e32 v233, 1.0, v233
	v_add_f32_e32 v234, 1.0, v234
	v_add_f32_e32 v235, 1.0, v235
	s_waitcnt lgkmcnt(3)
	v_mfma_f32_16x16x32_f16 v[144:147], v[12:15], v[206:209], v[222:225]
	v_rcp_f32_e32 v228, v228
	v_rcp_f32_e32 v229, v229
	v_rcp_f32_e32 v230, v230
	v_mfma_f32_16x16x32_f16 v[148:151], v[28:31], v[206:209], v[186:189]
	v_rcp_f32_e32 v231, v231
	v_fma_f32 v236, v228, v132, v138
	v_fma_f32 v237, v229, v133, v139
	v_fma_f32 v238, v230, v134, v140
	v_fma_f32 v239, v231, v135, v141
	v_mfma_f32_16x16x32_f16 v[152:155], v[32:35], v[206:209], v[80:83]
	v_mad_u32_u24 v253, v178, s17, v252
	ds_read_b128 v[116:119], v253 offset:24848
	ds_read_b128 v[120:123], v253 offset:24864
	ds_read_b128 v[138:141], v253 offset:24880
	ds_read_u16 v178, v176 offset:4
	v_exp_f32_e32 v236, v236
	v_exp_f32_e32 v237, v237
	v_exp_f32_e32 v238, v238
	s_waitcnt lgkmcnt(6)
	v_mfma_f32_16x16x32_f16 v[144:147], v[16:19], v[210:213], v[144:147]
	v_exp_f32_e32 v239, v239
	v_rcp_f32_e32 v232, v232
	v_rcp_f32_e32 v233, v233
	v_mfma_f32_16x16x32_f16 v[148:151], v[48:51], v[210:213], v[148:151]
	v_rcp_f32_e32 v234, v234
	v_rcp_f32_e32 v235, v235
	v_add_f32_e32 v236, 1.0, v236
	v_add_f32_e32 v237, 1.0, v237
	v_mfma_f32_16x16x32_f16 v[152:155], v[36:39], v[210:213], v[152:155]
	v_add_f32_e32 v238, 1.0, v238
	v_add_f32_e32 v239, 1.0, v239
	v_rcp_f32_e32 v236, v236
	v_rcp_f32_e32 v237, v237
	s_waitcnt lgkmcnt(5)
	v_mfma_f32_16x16x32_f16 v[144:147], v[20:23], v[214:217], v[144:147]
	v_rcp_f32_e32 v238, v238
	v_rcp_f32_e32 v239, v239
	v_pk_fma_f32 v[236:237], v[236:237], -2.0, 1.0 op_sel_hi:[1,0,0]
	v_pk_fma_f32 v[238:239], v[238:239], -2.0, 1.0 op_sel_hi:[1,0,0]
	v_mfma_f32_16x16x32_f16 v[148:151], v[52:55], v[214:217], v[148:151]
	v_pk_add_f32 v[240:241], v[172:173], v[236:237] neg_lo:[0,1] neg_hi:[0,1]
	v_pk_add_f32 v[242:243], v[174:175], v[238:239] neg_lo:[0,1] neg_hi:[0,1]
	v_pk_fma_f32 v[172:173], v[232:233], v[240:241], v[236:237]
	v_pk_fma_f32 v[174:175], v[234:235], v[242:243], v[238:239]
	v_cvt_pk_f16_f32 v244, v172, v173
	v_cvt_pk_f16_f32 v245, v174, v175
	ds_write_b64 v163, v[244:245]
	v_mfma_f32_16x16x32_f16 v[152:155], v[40:43], v[214:217], v[152:155]
	s_waitcnt lgkmcnt(5)
	v_mfma_f32_16x16x32_f16 v[144:147], v[24:27], v[218:221], v[144:147]
	v_mfma_f32_16x16x32_f16 v[148:151], v[56:59], v[218:221], v[148:151]
	v_mfma_f32_16x16x32_f16 v[152:155], v[44:47], v[218:221], v[152:155]
	s_waitcnt lgkmcnt(0)
	s_barrier
	ds_read_b128 v[190:193], v156 offset:0
	ds_read_b128 v[194:197], v156 offset:1024
	ds_read_b128 v[198:201], v156 offset:2048
	ds_read_b128 v[202:205], v156 offset:3072
	v_mfma_f32_16x16x32_f16 v[92:95], v[72:75], v[206:209], v[92:95]
	v_exp_f32_e32 v228, v144
	v_exp_f32_e32 v229, v145
	v_exp_f32_e32 v230, v146
	v_mfma_f32_16x16x32_f16 v[92:95], v[8:11], v[210:213], v[92:95]
	v_exp_f32_e32 v231, v147
	v_exp_f32_e32 v232, v148
	v_exp_f32_e32 v233, v149
	v_mfma_f32_16x16x32_f16 v[92:95], v[4:7], v[214:217], v[92:95]
	v_exp_f32_e32 v234, v150
	v_exp_f32_e32 v235, v151
	v_add_f32_e32 v228, 1.0, v228
	v_add_f32_e32 v229, 1.0, v229
	v_mfma_f32_16x16x32_f16 v[92:95], v[0:3], v[218:221], v[92:95]
	s_ashr_i32 s9, s8, 31
	s_lshl_b64 s[12:13], s[8:9], 15
	v_lshl_add_u64 v[246:247], v[158:159], 0, s[12:13]
	global_load_dwordx4 v[72:75], v[246:247], off
	global_load_dwordx4 v[8:11], v[246:247], off offset:1024
	global_load_dwordx4 v[4:7], v[246:247], off offset:2048
	global_load_dwordx4 v[0:3], v[246:247], off offset:3072
	v_add_f32_e32 v230, 1.0, v230
	v_add_f32_e32 v231, 1.0, v231
	v_add_f32_e32 v232, 1.0, v232
	v_add_f32_e32 v233, 1.0, v233
	v_add_f32_e32 v234, 1.0, v234
	v_add_f32_e32 v235, 1.0, v235
	s_waitcnt lgkmcnt(3)
	v_mfma_f32_16x16x32_f16 v[124:127], v[12:15], v[190:193], v[116:119]
	v_rcp_f32_e32 v228, v228
	v_rcp_f32_e32 v229, v229
	v_rcp_f32_e32 v230, v230
	v_mfma_f32_16x16x32_f16 v[128:131], v[28:31], v[190:193], v[120:123]
	v_rcp_f32_e32 v231, v231
	v_fma_f32 v236, v228, v152, v182
	v_fma_f32 v237, v229, v153, v183
	v_fma_f32 v238, v230, v154, v184
	v_fma_f32 v239, v231, v155, v185
	v_mfma_f32_16x16x32_f16 v[132:135], v[32:35], v[190:193], v[80:83]
	v_mad_u32_u24 v253, v177, s17, v252
	ds_read_b128 v[222:225], v253 offset:24848
	ds_read_b128 v[186:189], v253 offset:24864
	ds_read_b128 v[182:185], v253 offset:24880
	ds_read_u16 v177, v176 offset:4164
	v_exp_f32_e32 v236, v236
	v_exp_f32_e32 v237, v237
	v_exp_f32_e32 v238, v238
	s_waitcnt lgkmcnt(6)
	v_mfma_f32_16x16x32_f16 v[124:127], v[16:19], v[194:197], v[124:127]
	v_exp_f32_e32 v239, v239
	v_rcp_f32_e32 v232, v232
	v_rcp_f32_e32 v233, v233
	v_mfma_f32_16x16x32_f16 v[128:131], v[48:51], v[194:197], v[128:131]
	v_rcp_f32_e32 v234, v234
	v_rcp_f32_e32 v235, v235
	v_add_f32_e32 v236, 1.0, v236
	v_add_f32_e32 v237, 1.0, v237
	v_mfma_f32_16x16x32_f16 v[132:135], v[36:39], v[194:197], v[132:135]
	v_add_f32_e32 v238, 1.0, v238
	v_add_f32_e32 v239, 1.0, v239
	v_rcp_f32_e32 v236, v236
	v_rcp_f32_e32 v237, v237
	s_waitcnt lgkmcnt(5)
	v_mfma_f32_16x16x32_f16 v[124:127], v[20:23], v[198:201], v[124:127]
	v_rcp_f32_e32 v238, v238
	v_rcp_f32_e32 v239, v239
	v_pk_fma_f32 v[236:237], v[236:237], -2.0, 1.0 op_sel_hi:[1,0,0]
	v_pk_fma_f32 v[238:239], v[238:239], -2.0, 1.0 op_sel_hi:[1,0,0]
	v_mfma_f32_16x16x32_f16 v[128:131], v[52:55], v[198:201], v[128:131]
	v_pk_add_f32 v[240:241], v[168:169], v[236:237] neg_lo:[0,1] neg_hi:[0,1]
	v_pk_add_f32 v[242:243], v[170:171], v[238:239] neg_lo:[0,1] neg_hi:[0,1]
	v_pk_fma_f32 v[168:169], v[232:233], v[240:241], v[236:237]
	v_pk_fma_f32 v[170:171], v[234:235], v[242:243], v[238:239]
	v_cvt_pk_f16_f32 v244, v168, v169
	v_cvt_pk_f16_f32 v245, v170, v171
	ds_write_b64 v163, v[244:245] offset:4096
	v_mfma_f32_16x16x32_f16 v[132:135], v[40:43], v[198:201], v[132:135]
	s_waitcnt lgkmcnt(5)
	v_mfma_f32_16x16x32_f16 v[124:127], v[24:27], v[202:205], v[124:127]
	v_mfma_f32_16x16x32_f16 v[128:131], v[56:59], v[202:205], v[128:131]
	v_mfma_f32_16x16x32_f16 v[132:135], v[44:47], v[202:205], v[132:135]
	s_waitcnt lgkmcnt(0)
	s_barrier
	ds_read_b128 v[206:209], v156 offset:4096
	ds_read_b128 v[210:213], v156 offset:5120
	ds_read_b128 v[214:217], v156 offset:6144
	ds_read_b128 v[218:221], v156 offset:7168
	s_waitcnt vmcnt(4)
	v_mfma_f32_16x16x32_f16 v[96:99], v[112:115], v[190:193], v[96:99]
	v_exp_f32_e32 v228, v124
	v_exp_f32_e32 v229, v125
	v_exp_f32_e32 v230, v126
	v_mfma_f32_16x16x32_f16 v[96:99], v[108:111], v[194:197], v[96:99]
	v_exp_f32_e32 v231, v127
	v_exp_f32_e32 v232, v128
	v_exp_f32_e32 v233, v129
	v_mfma_f32_16x16x32_f16 v[96:99], v[104:107], v[198:201], v[96:99]
	v_exp_f32_e32 v234, v130
	v_exp_f32_e32 v235, v131
	v_add_f32_e32 v228, 1.0, v228
	v_add_f32_e32 v229, 1.0, v229
	v_mfma_f32_16x16x32_f16 v[96:99], v[100:103], v[202:205], v[96:99]
	v_add_f32_e32 v230, 1.0, v230
	v_add_f32_e32 v231, 1.0, v231
	v_add_f32_e32 v232, 1.0, v232
	v_add_f32_e32 v233, 1.0, v233
	v_add_f32_e32 v234, 1.0, v234
	v_add_f32_e32 v235, 1.0, v235
	s_waitcnt lgkmcnt(3)
	v_mfma_f32_16x16x32_f16 v[144:147], v[12:15], v[206:209], v[222:225]
	v_rcp_f32_e32 v228, v228
	v_rcp_f32_e32 v229, v229
	v_rcp_f32_e32 v230, v230
	v_mfma_f32_16x16x32_f16 v[148:151], v[28:31], v[206:209], v[186:189]
	v_rcp_f32_e32 v231, v231
	v_fma_f32 v236, v228, v132, v138
	v_fma_f32 v237, v229, v133, v139
	v_fma_f32 v238, v230, v134, v140
	v_fma_f32 v239, v231, v135, v141
	v_mfma_f32_16x16x32_f16 v[152:155], v[32:35], v[206:209], v[80:83]
	v_mad_u32_u24 v253, v178, s17, v252
	ds_read_b128 v[116:119], v253 offset:24848
	ds_read_b128 v[120:123], v253 offset:24864
	ds_read_b128 v[138:141], v253 offset:24880
	ds_read_u16 v178, v176 offset:6
	v_exp_f32_e32 v236, v236
	v_exp_f32_e32 v237, v237
	v_exp_f32_e32 v238, v238
	s_waitcnt lgkmcnt(6)
	v_mfma_f32_16x16x32_f16 v[144:147], v[16:19], v[210:213], v[144:147]
	v_exp_f32_e32 v239, v239
	v_rcp_f32_e32 v232, v232
	v_rcp_f32_e32 v233, v233
	v_mfma_f32_16x16x32_f16 v[148:151], v[48:51], v[210:213], v[148:151]
	v_rcp_f32_e32 v234, v234
	v_rcp_f32_e32 v235, v235
	v_add_f32_e32 v236, 1.0, v236
	v_add_f32_e32 v237, 1.0, v237
	v_mfma_f32_16x16x32_f16 v[152:155], v[36:39], v[210:213], v[152:155]
	v_add_f32_e32 v238, 1.0, v238
	v_add_f32_e32 v239, 1.0, v239
	v_rcp_f32_e32 v236, v236
	v_rcp_f32_e32 v237, v237
	s_waitcnt lgkmcnt(5)
	v_mfma_f32_16x16x32_f16 v[144:147], v[20:23], v[214:217], v[144:147]
	v_rcp_f32_e32 v238, v238
	v_rcp_f32_e32 v239, v239
	v_pk_fma_f32 v[236:237], v[236:237], -2.0, 1.0 op_sel_hi:[1,0,0]
	v_pk_fma_f32 v[238:239], v[238:239], -2.0, 1.0 op_sel_hi:[1,0,0]
	v_mfma_f32_16x16x32_f16 v[148:151], v[52:55], v[214:217], v[148:151]
	v_pk_add_f32 v[240:241], v[172:173], v[236:237] neg_lo:[0,1] neg_hi:[0,1]
	v_pk_add_f32 v[242:243], v[174:175], v[238:239] neg_lo:[0,1] neg_hi:[0,1]
	v_pk_fma_f32 v[172:173], v[232:233], v[240:241], v[236:237]
	v_pk_fma_f32 v[174:175], v[234:235], v[242:243], v[238:239]
	v_cvt_pk_f16_f32 v244, v172, v173
	v_cvt_pk_f16_f32 v245, v174, v175
	ds_write_b64 v163, v[244:245]
	v_mfma_f32_16x16x32_f16 v[152:155], v[40:43], v[214:217], v[152:155]
	s_waitcnt lgkmcnt(5)
	v_mfma_f32_16x16x32_f16 v[144:147], v[24:27], v[218:221], v[144:147]
	v_mfma_f32_16x16x32_f16 v[148:151], v[56:59], v[218:221], v[148:151]
	v_mfma_f32_16x16x32_f16 v[152:155], v[44:47], v[218:221], v[152:155]
	s_add_i32 s5, s5, 2
	s_add_i32 s8, s8, s4
	v_add_u32_e32 v176, 4, v176
	v_lshl_add_u64 v[166:167], v[166:167], 0, s[6:7]
	s_cmpk_gt_u32 s5, 0x7d
	s_waitcnt lgkmcnt(0)
	s_barrier
	s_cbranch_scc0 .Lgru_loop
	s_waitcnt vmcnt(0)
	v_mfma_f32_16x16x32_f16 v[92:95], v[112:115], v[206:209], v[92:95]
	v_mfma_f32_16x16x32_f16 v[92:95], v[108:111], v[210:213], v[92:95]
	v_mfma_f32_16x16x32_f16 v[92:95], v[104:107], v[214:217], v[92:95]
	v_mfma_f32_16x16x32_f16 v[92:95], v[100:103], v[218:221], v[92:95]
	ds_read_b128 v[190:193], v156 offset:0
	ds_read_b128 v[194:197], v156 offset:1024
	ds_read_b128 v[198:201], v156 offset:2048
	ds_read_b128 v[202:205], v156 offset:3072
	v_exp_f32_e32 v228, v144
	v_exp_f32_e32 v229, v145
	v_exp_f32_e32 v230, v146
	v_exp_f32_e32 v231, v147
	v_exp_f32_e32 v232, v148
	v_exp_f32_e32 v233, v149
	v_exp_f32_e32 v234, v150
	v_exp_f32_e32 v235, v151
	v_add_f32_e32 v228, 1.0, v228
	v_add_f32_e32 v229, 1.0, v229
	v_add_f32_e32 v230, 1.0, v230
	v_add_f32_e32 v231, 1.0, v231
	v_add_f32_e32 v232, 1.0, v232
	v_add_f32_e32 v233, 1.0, v233
	v_add_f32_e32 v234, 1.0, v234
	v_add_f32_e32 v235, 1.0, v235
	v_rcp_f32_e32 v228, v228
	v_rcp_f32_e32 v229, v229
	v_rcp_f32_e32 v230, v230
	v_rcp_f32_e32 v231, v231
	v_fma_f32 v236, v228, v152, v182
	v_fma_f32 v237, v229, v153, v183
	v_fma_f32 v238, v230, v154, v184
	v_fma_f32 v239, v231, v155, v185
	v_exp_f32_e32 v236, v236
	v_exp_f32_e32 v237, v237
	v_exp_f32_e32 v238, v238
	v_exp_f32_e32 v239, v239
	v_rcp_f32_e32 v232, v232
	v_rcp_f32_e32 v233, v233
	v_rcp_f32_e32 v234, v234
	v_rcp_f32_e32 v235, v235
	v_add_f32_e32 v236, 1.0, v236
	v_add_f32_e32 v237, 1.0, v237
	v_add_f32_e32 v238, 1.0, v238
	v_add_f32_e32 v239, 1.0, v239
	v_rcp_f32_e32 v236, v236
	v_rcp_f32_e32 v237, v237
	v_rcp_f32_e32 v238, v238
	v_rcp_f32_e32 v239, v239
	v_pk_fma_f32 v[236:237], v[236:237], -2.0, 1.0 op_sel_hi:[1,0,0]
	v_pk_fma_f32 v[238:239], v[238:239], -2.0, 1.0 op_sel_hi:[1,0,0]
	v_pk_add_f32 v[240:241], v[168:169], v[236:237] neg_lo:[0,1] neg_hi:[0,1]
	v_pk_add_f32 v[242:243], v[170:171], v[238:239] neg_lo:[0,1] neg_hi:[0,1]
	v_pk_fma_f32 v[168:169], v[232:233], v[240:241], v[236:237]
	v_pk_fma_f32 v[170:171], v[234:235], v[242:243], v[238:239]
	v_cvt_pk_f16_f32 v244, v168, v169
	v_cvt_pk_f16_f32 v245, v170, v171
	ds_write_b64 v163, v[244:245] offset:4096
	s_waitcnt lgkmcnt(1)
	v_mfma_f32_16x16x32_f16 v[96:99], v[72:75], v[190:193], v[96:99]
	v_mfma_f32_16x16x32_f16 v[96:99], v[8:11], v[194:197], v[96:99]
	v_mfma_f32_16x16x32_f16 v[96:99], v[4:7], v[198:201], v[96:99]
	v_mfma_f32_16x16x32_f16 v[96:99], v[0:3], v[202:205], v[96:99]
	s_waitcnt lgkmcnt(0)
	s_barrier
	ds_read_b128 v[206:209], v156 offset:4096
	ds_read_b128 v[210:213], v156 offset:5120
	ds_read_b128 v[214:217], v156 offset:6144
	ds_read_b128 v[218:221], v156 offset:7168
	s_lshl_b32 s0, s16, 21
	s_add_u32 s4, s10, s0
	s_addc_u32 s5, s11, 0
	s_lshl_b64 s[0:1], s[2:3], 9
	s_add_u32 s0, s4, s0
	s_addc_u32 s1, s5, s1
	v_lshlrev_b32_e32 v222, 9, v161
	v_mov_b32_e32 v223, 0
	v_lshlrev_b32_e32 v224, 2, v162
	v_mov_b32_e32 v225, 0
	v_lshl_add_u64 v[186:187], s[0:1], 0, v[224:225]
	v_lshlrev_b32_e32 v224, 2, v160
	v_lshl_add_u64 v[186:187], v[186:187], 0, v[224:225]
	v_lshl_add_u64 v[188:189], v[186:187], 0, v[222:223]
	v_or_b32_e32 v222, 0x2000, v222
	v_lshl_add_u64 v[246:247], v[186:187], 0, v[222:223]
	s_waitcnt lgkmcnt(0)
	v_mfma_f32_16x16x32_f16 v[92:95], v[72:75], v[206:209], v[92:95]
	v_mfma_f32_16x16x32_f16 v[92:95], v[8:11], v[210:213], v[92:95]
	v_mfma_f32_16x16x32_f16 v[92:95], v[4:7], v[214:217], v[92:95]
	v_mfma_f32_16x16x32_f16 v[92:95], v[0:3], v[218:221], v[92:95]
	s_nop 7
	s_nop 3
	global_store_dwordx4 v[188:189], v[96:99], off
	global_store_dwordx4 v[246:247], v[92:95], off
	s_endpgm

	.amdhsa_kernel _Z10gru_kernelPKhPf
		.amdhsa_group_segment_fixed_size 125728
		.amdhsa_private_segment_fixed_size 0
		.amdhsa_kernarg_size 16
		.amdhsa_user_sgpr_count 2
		.amdhsa_user_sgpr_dispatch_ptr 0
		.amdhsa_user_sgpr_queue_ptr 0
		.amdhsa_user_sgpr_kernarg_segment_ptr 1
		.amdhsa_user_sgpr_dispatch_id 0
		.amdhsa_user_sgpr_kernarg_preload_length 0
		.amdhsa_user_sgpr_kernarg_preload_offset 0
		.amdhsa_user_sgpr_private_segment_size 0
		.amdhsa_uses_dynamic_stack 0
		.amdhsa_enable_private_segment 0
		.amdhsa_system_sgpr_workgroup_id_x 1
		.amdhsa_system_sgpr_workgroup_id_y 0
		.amdhsa_system_sgpr_workgroup_id_z 0
		.amdhsa_system_sgpr_workgroup_info 0
		.amdhsa_system_vgpr_workitem_id 0
		.amdhsa_next_free_vgpr 254
		.amdhsa_next_free_sgpr 19
		.amdhsa_accum_offset 256
		.amdhsa_reserve_vcc 1
		.amdhsa_float_round_mode_32 0
		.amdhsa_float_round_mode_16_64 0
		.amdhsa_float_denorm_mode_32 3
		.amdhsa_float_denorm_mode_16_64 3
		.amdhsa_dx10_clamp 1
		.amdhsa_ieee_mode 1
		.amdhsa_fp16_overflow 0
		.amdhsa_tg_split 0
		.amdhsa_exception_fp_ieee_invalid_op 0
		.amdhsa_exception_fp_denorm_src 0
		.amdhsa_exception_fp_ieee_div_zero 0
		.amdhsa_exception_fp_ieee_overflow 0
		.amdhsa_exception_fp_ieee_underflow 0
		.amdhsa_exception_fp_ieee_inexact 0
		.amdhsa_exception_int_div_zero 0
	.end_amdhsa_kernel

.Lfunc_end1:
	.size	_Z10gru_kernelPKhPf, .Lfunc_end1-_Z10gru_kernelPKhPf
	.set _Z10gru_kernelPKhPf.num_vgpr, 254
	.set _Z10gru_kernelPKhPf.num_agpr, 0
	.set _Z10gru_kernelPKhPf.numbered_sgpr, 19
	.set _Z10gru_kernelPKhPf.num_named_barrier, 0
	.set _Z10gru_kernelPKhPf.private_seg_size, 0
	.set _Z10gru_kernelPKhPf.uses_vcc, 1
	.set _Z10gru_kernelPKhPf.uses_flat_scratch, 0
	.set _Z10gru_kernelPKhPf.has_dyn_sized_stack, 0
	.set _Z10gru_kernelPKhPf.has_recursion, 0
	.set _Z10gru_kernelPKhPf.has_indirect_call, 0

amdhsa.kernels:
  - .agpr_count:     0
    .args:
      - .actual_access:  read_only
        .address_space:  global
        .offset:         0
        .size:           8
        .value_kind:     global_buffer
      - .actual_access:  read_only
        .address_space:  global
        .offset:         8
        .size:           8
        .value_kind:     global_buffer
      - .actual_access:  read_only
        .address_space:  global
        .offset:         16
        .size:           8
        .value_kind:     global_buffer
      - .actual_access:  read_only
        .address_space:  global
        .offset:         24
        .size:           8
        .value_kind:     global_buffer
      - .actual_access:  read_only
        .address_space:  global
        .offset:         32
        .size:           8
        .value_kind:     global_buffer
      - .actual_access:  read_only
        .address_space:  global
        .offset:         40
        .size:           8
        .value_kind:     global_buffer
      - .actual_access:  read_only
        .address_space:  global
        .offset:         48
        .size:           8
        .value_kind:     global_buffer
      - .actual_access:  read_only
        .address_space:  global
        .offset:         56
        .size:           8
        .value_kind:     global_buffer
      - .actual_access:  read_only
        .address_space:  global
        .offset:         64
        .size:           8
        .value_kind:     global_buffer
      - .actual_access:  read_only
        .address_space:  global
        .offset:         72
        .size:           8
        .value_kind:     global_buffer
      - .actual_access:  read_only
        .address_space:  global
        .offset:         80
        .size:           8
        .value_kind:     global_buffer
      - .actual_access:  write_only
        .address_space:  global
        .offset:         88
        .size:           8
        .value_kind:     global_buffer
    .group_segment_fixed_size: 512
    .kernarg_segment_align: 8
    .kernarg_segment_size: 96
    .language:       OpenCL C
    .language_version:
      - 2
      - 0
    .max_flat_workgroup_size: 256
    .name:           _Z11prep_kernelPKiS0_PKfS2_S2_S2_S2_S2_S2_S2_S2_Ph
    .private_segment_fixed_size: 0
    .sgpr_count:     22
    .sgpr_spill_count: 0
    .symbol:         _Z11prep_kernelPKiS0_PKfS2_S2_S2_S2_S2_S2_S2_S2_Ph.kd
    .uniform_work_group_size: 1
    .uses_dynamic_stack: false
    .vgpr_count:     16
    .vgpr_spill_count: 0
    .wavefront_size: 64
  - .agpr_count:     0
    .args:
      - .actual_access:  read_only
        .address_space:  global
        .offset:         0
        .size:           8
        .value_kind:     global_buffer
      - .actual_access:  write_only
        .address_space:  global
        .offset:         8
        .size:           8
        .value_kind:     global_buffer
    .group_segment_fixed_size: 125728
    .kernarg_segment_align: 8
    .kernarg_segment_size: 16
    .language:       OpenCL C
    .language_version:
      - 2
      - 0
    .max_flat_workgroup_size: 512
    .name:           _Z10gru_kernelPKhPf
    .private_segment_fixed_size: 0
    .sgpr_count:     25
    .sgpr_spill_count: 0
    .symbol:         _Z10gru_kernelPKhPf.kd
    .uniform_work_group_size: 1
    .uses_dynamic_stack: false
    .vgpr_count:     254
    .vgpr_spill_count: 0
    .wavefront_size: 64
  - .agpr_count:     0
    .args:
      - .actual_access:  read_only
        .address_space:  global
        .offset:         0
        .size:           8
        .value_kind:     global_buffer
      - .actual_access:  read_only
        .address_space:  global
        .offset:         8
        .size:           8
        .value_kind:     global_buffer
      - .actual_access:  write_only
        .address_space:  global
        .offset:         16
        .size:           8
        .value_kind:     global_buffer
    .group_segment_fixed_size: 0
    .kernarg_segment_align: 8
    .kernarg_segment_size: 24
    .language:       OpenCL C
    .language_version:
      - 2
      - 0
    .max_flat_workgroup_size: 256
    .name:           _Z12final_kernelPKfS0_Pf
    .private_segment_fixed_size: 0
    .sgpr_count:     16
    .sgpr_spill_count: 0
    .symbol:         _Z12final_kernelPKfS0_Pf.kd
    .uniform_work_group_size: 1
    .uses_dynamic_stack: false
    .vgpr_count:     26
    .vgpr_spill_count: 0
    .wavefront_size: 64
